# ILC6-nt + MLA K/V ring 3 buffers with DMA prefetch distance 2 (tile DMA and converter loads both stay in flight across the per-tile wait)
# speedup vs baseline: 1.0039x; 1.0039x over previous
;     ...
;     int tid = tid_x(); asm volatile("" : "+v"(tid));
;     const int wid = tid >> 6, lane = tid & 63, r32 = lane & 31, hi = lane >> 5;
;     const int qb = uid & 15, h = (uid >> 4) % NH, b = (uid >> 4) / NH;
;     const int tok0 = b * SEQ;
;     const int qrow = tok0 + qb * 256 + wid * 32 + r32;
;     LAS char* V_lds = lds + LDS_VBUF; LAS char* K_lds = lds + LDS_KBUF;
;     LAS float* ws = (LAS float*)(lds + LDS_WS) + wid * 64; LAS float* li_l = ws; LAS float* al_l = ws + 32;
;     LAS float* rpbL = (LAS float*)(lds + LDS_RPB);
;     const int sr = tid >> 4, sc = (tid & 15) * 8, vst0 = v_st(sr, sc), vst1 = v_st(32 + sr, sc);
;     const int sr64 = tid >> 3, sc64 = (tid & 7) * 8;
;     const int vb0 = (int)(unsigned)(uintptr_t)V_lds + v_rd_base(lane);
;     int NT = 64, kbase = tok0;
;     int rq = 0, qc = 0, kr_lo = 0;
;     if constexpr (MODE == MODE_NA) { const int rq0 = qb * 4; kr_lo = min(min(max(rq0 - 4, 0), 56), 52); NT = 12; kbase = tok0 + kr_lo * 64; rq = rq0 + (wid >> 1); qc = (wid & 1) * 32 + r32;
;         for (int i = tid; i < 15 * 31; i += 512) rpbL[i] = P.rpb[h * 465 + i];
;         __syncthreads(); }
;     const bf16* Kg; const bf16* Vg; const bf16* Kg2 = nullptr; int ldk, ldv;
;     if constexpr (MODE == MODE_MLA) { Kg = P.KVM + h * 256; Vg = P.KVM + h * 256 + 128; Kg2 = P.U + U_KR; ldk = KVW; ldv = KVW; }
;     else if constexpr (MODE == MODE_NA) { Kg = P.U + U_NA + 512 + h * 128; Vg = P.U + U_NA + 1024 + h * 128; ldk = UW; ldv = UW; }
;     else { Kg = P.U + U_DF + 512 + h * 128; Vg = P.U + U_DF + 1024 + h * 128; ldk = UW; ldv = UW; }
;     constexpr int pass = PASS;
;     constexpr bool HALF_OFFSET = false;
;     {
;         float m_reg = -1e30f, l_reg = 0; f32x16 o[4] = {}; bf16x8 qr[NQ];
;         if constexpr (MODE == MODE_MLA) {
;             const bf16* Qw = P.QM + (size_t)qrow * QMW + h * 192 + hi * 8;
; #pragma unroll
;             for (int d0 = 0; d0 < 12; ++d0) qr[d0] = *(const bf16x8*)(Qw + d0 * 16);
;             const f32x2* rt = P.ropeM + (size_t)(qrow & (SEQ - 1)) * 32;
; #pragma unroll
;             for (int g = 0; g < 2; ++g) {
;                 bf16x8 x1 = qr[8 + g], x2 = qr[10 + g];
; #pragma unroll
;                 for (int e = 0; e < 8; ++e) { const f32x2 cs = rt[g * 16 + hi * 8 + e];
;                     const float a = bf2f((unsigned short)x1[e]), c = bf2f((unsigned short)x2[e]);
.LBB0_785:
	s_lshl_b32 s0, s22, 1
	s_and_b32 s0, s0, 14
	s_ashr_i32 s1, s22, 7
	s_add_i32 s0, s0, s1
	s_getreg_b32 s1, hwreg(HW_REG_HW_ID, 0, 6)
	s_and_b32 s1, s1, 63
	s_lshl_b32 s1, s1, 2
	s_add_i32 s1, s1, 0
	s_add_i32 s1, s1, 0x23f00
	s_waitcnt vmcnt(15)
	v_mov_b32_e32 v0, s1
	ds_read_b32 v0, v0
	v_mbcnt_lo_u32_b32 v1, -1, 0
	v_mbcnt_hi_u32_b32 v1, -1, v1
	v_mov_b32_e32 v145, v193
	v_mov_b32_e32 v149, v193
	s_movk_i32 s3, 0x70
	s_waitcnt lgkmcnt(0)
	v_readfirstlane_b32 s1, v0
	s_mov_b32 s28, 0
	s_and_b32 s39, s74, 63
	s_lshl_b32 s39, s39, 3
	s_add_u32 s39, s39, s1
	s_lshr_b32 s54, s74, 6
	v_lshrrev_b32_e32 v226, 3, v1
	v_and_b32_e32 v229, 7, v1
	v_readlane_b32 s56, v254, 60
	s_lshr_b32 s52, s1, 2
	s_mul_i32 s52, s52, 31
	s_add_u32 s52, s52, 31
	s_mov_b32 s42, 0
	s_mov_b32 s51, 16
	s_mov_b32 s53, 0
	v_mov_b32_e32 v147, v193
	s_waitcnt vmcnt(13)
	v_lshl_add_u32 v11, s1, 6, v1
	s_lshr_b32 s1, s0, 29
	s_add_i32 s1, s0, s1
	s_and_b32 s2, s1, -8
	s_sub_i32 s23, s0, s2
	s_lshl_b32 s0, s1, 9
	s_and_b32 s4, s0, 0xfffff000
	s_lshl_b32 s0, s22, 5
	s_and_b32 s0, s0, 0xf00
	s_or_b32 s25, s4, s0
	v_ashrrev_i32_e32 v156, 6, v11
	v_and_b32_e32 v154, 31, v11
	v_lshl_add_u32 v0, v156, 5, s25
	v_or_b32_e32 v8, v0, v154
	v_and_b32_e32 v0, 0x3fffffc0, v11
	s_add_i32 s0, 0, 0x1e000
	v_lshl_add_u32 v157, v0, 2, s0
	s_lshl_b32 s0, s23, 8
	s_ashr_i32 s1, s0, 31
	s_lshl_b64 s[0:1], s[0:1], 1
	s_add_u32 s26, s18, s0
	v_mov_b64_e32 v[0:1], s[10:11]
	s_movk_i32 s0, 0xc00
	s_addc_u32 s27, s19, s1
	v_mad_i64_i32 v[0:1], s[0:1], v8, s0, v[0:1]
	s_mul_i32 s0, s23, 0xc0
	v_lshlrev_b32_e32 v8, 8, v8
	v_bfe_u32 v155, v11, 5, 1
	s_ashr_i32 s1, s0, 31
	v_and_b32_e32 v192, 0xfff00, v8
	v_lshl_add_u64 v[0:1], s[0:1], 1, v[0:1]
	v_lshlrev_b32_e32 v144, 4, v155
	v_lshl_add_u64 v[8:9], s[12:13], 0, v[192:193]
	v_lshlrev_b32_e32 v192, 6, v155
	v_lshl_add_u64 v[4:5], v[0:1], 0, v[144:145]
	v_lshl_add_u64 v[8:9], v[8:9], 0, v[192:193]
	global_load_dwordx4 v[96:99], v[4:5], off
	global_load_dwordx4 v[100:103], v[4:5], off offset:32
	global_load_dwordx4 v[104:107], v[4:5], off offset:64
	global_load_dwordx4 v[108:111], v[4:5], off offset:96
	global_load_dwordx4 v[112:115], v[4:5], off offset:128
	global_load_dwordx4 v[116:119], v[4:5], off offset:160
	global_load_dwordx4 v[120:123], v[4:5], off offset:192
	global_load_dwordx4 v[124:127], v[4:5], off offset:224
	global_load_dwordx4 v[26:29], v[4:5], off offset:256
	global_load_dwordx4 v[0:3], v[4:5], off offset:288
	global_load_dwordx4 v[30:33], v[4:5], off offset:320
	s_nop 0
	global_load_dwordx4 v[4:7], v[4:5], off offset:352
	s_waitcnt vmcnt(24)
	v_lshlrev_b32_e32 v13, 4, v11
	global_load_dwordx2 v[14:15], v[8:9], off
	v_readfirstlane_b32 s0, v156
	s_ashr_i32 s5, s4, 31
	s_lshl_b32 s2, s0, 10
	s_lshl_b64 s[0:1], s[4:5], 12
	s_add_u32 s0, s26, s0
	s_addc_u32 s1, s27, s1
	s_add_i32 s29, s2, 0
	s_mov_b32 m0, s29
	s_add_i32 s2, s29, 0xc000
	v_and_b32_e32 v10, 63, v11
	v_and_b32_e32 v12, 0xc0, v13
	v_mov_b32_e32 v151, v193
	v_lshlrev_b32_e32 v145, 8, v154
	v_lshlrev_b32_e32 v167, 7, v154
	v_lshl_add_u32 v163, v154, 2, v157
	v_mov_b32_e32 v174, 0
	v_mov_b32_e32 v173, 0xf149f2ca
	s_waitcnt vmcnt(4)
	v_lshlrev_b32_e32 v17, 16, v26
	s_waitcnt vmcnt(2)
	v_lshlrev_b32_e32 v16, 16, v30
	s_waitcnt vmcnt(0)
	v_pk_mul_f32 v[18:19], v[14:15], v[16:17] op_sel:[0,1] op_sel_hi:[1,0]
	v_pk_mul_f32 v[14:15], v[14:15], v[16:17]
	v_sub_f32_e32 v18, v18, v19
	v_add_f32_e32 v14, v15, v14
	v_cvt_pk_bf16_f32 v15, v18, v193
	v_cvt_pk_bf16_f32 v14, v14, v193
	global_load_dwordx2 v[16:17], v[8:9], off offset:8
	v_and_b32_e32 v19, 0xffff0000, v26
	v_and_b32_e32 v18, 0xffff0000, v30
	s_waitcnt vmcnt(0)
	v_pk_mul_f32 v[20:21], v[16:17], v[18:19] op_sel:[0,1] op_sel_hi:[1,0]
	v_pk_mul_f32 v[16:17], v[16:17], v[18:19]
	v_sub_f32_e32 v20, v20, v21
	v_add_f32_e32 v16, v16, v17
	v_cvt_pk_bf16_f32 v17, v20, v193
	v_cvt_pk_bf16_f32 v16, v16, v193
	global_load_dwordx2 v[18:19], v[8:9], off offset:16
	v_lshlrev_b32_e32 v21, 16, v27
	v_lshlrev_b32_e32 v20, 16, v31
	s_waitcnt vmcnt(0)
	v_pk_mul_f32 v[22:23], v[18:19], v[20:21] op_sel:[0,1] op_sel_hi:[1,0]
	v_pk_mul_f32 v[18:19], v[18:19], v[20:21]
	v_sub_f32_e32 v22, v22, v23
	v_add_f32_e32 v18, v18, v19
	v_cvt_pk_bf16_f32 v19, v22, v193
	v_cvt_pk_bf16_f32 v18, v18, v193
	global_load_dwordx2 v[20:21], v[8:9], off offset:24
	v_and_b32_e32 v23, 0xffff0000, v27
	v_and_b32_e32 v22, 0xffff0000, v31
	s_waitcnt vmcnt(0)
	v_pk_mul_f32 v[24:25], v[20:21], v[22:23] op_sel:[0,1] op_sel_hi:[1,0]
	v_pk_mul_f32 v[20:21], v[20:21], v[22:23]
	v_sub_f32_e32 v24, v24, v25
	v_add_f32_e32 v20, v20, v21
	v_cvt_pk_bf16_f32 v21, v24, v193
	v_cvt_pk_bf16_f32 v20, v20, v193
	global_load_dwordx2 v[22:23], v[8:9], off offset:32
	v_lshlrev_b32_e32 v25, 16, v28
	v_lshlrev_b32_e32 v24, 16, v32
	s_waitcnt vmcnt(0)
	v_pk_mul_f32 v[26:27], v[22:23], v[24:25] op_sel:[0,1] op_sel_hi:[1,0]
	v_pk_mul_f32 v[22:23], v[22:23], v[24:25]
	v_sub_f32_e32 v26, v26, v27
	v_add_f32_e32 v22, v22, v23
	v_cvt_pk_bf16_f32 v23, v26, v193
	v_cvt_pk_bf16_f32 v22, v22, v193
	global_load_dwordx2 v[24:25], v[8:9], off offset:40
	v_and_b32_e32 v27, 0xffff0000, v28
	v_and_b32_e32 v26, 0xffff0000, v32
	s_waitcnt vmcnt(0)
	v_pk_mul_f32 v[30:31], v[24:25], v[26:27] op_sel:[0,1] op_sel_hi:[1,0]
	v_pk_mul_f32 v[24:25], v[24:25], v[26:27]
	v_sub_f32_e32 v28, v30, v31
	v_add_f32_e32 v24, v24, v25
	v_cvt_pk_bf16_f32 v25, v28, v193
	v_cvt_pk_bf16_f32 v24, v24, v193
	global_load_dwordx2 v[26:27], v[8:9], off offset:48
	v_lshlrev_b32_e32 v31, 16, v29
	v_lshlrev_b32_e32 v30, 16, v33
	v_and_b32_e32 v29, 0xffff0000, v29
	s_waitcnt vmcnt(0)
; __device__ __forceinline__ unsigned cvt_pk_bf16(float lo, float hi) { unsigned r; asm volatile("v_cvt_pk_bf16_f32 %0, %1, %2" : "=v"(r) : "v"(lo), "v"(hi)); return r; }
;     ...
;             const f32x2* rt = P.ropeM + (size_t)(qrow & (SEQ - 1)) * 32;
; #pragma unroll
;             for (int g = 0; g < 2; ++g) {
;                 bf16x8 x1 = qr[8 + g], x2 = qr[10 + g];
; #pragma unroll
;                 for (int e = 0; e < 8; ++e) { const f32x2 cs = rt[g * 16 + hi * 8 + e];
;                     const float a = bf2f((unsigned short)x1[e]), c = bf2f((unsigned short)x2[e]);
;                     const float ra = a * cs.x - c * cs.y, rc = c * cs.x + a * cs.y;
;                     x1[e] = (short)(cvt_pk_bf16(ra, 0.f) & 0xffffu); x2[e] = (short)(cvt_pk_bf16(rc, 0.f) & 0xffffu); }
;                 qr[8 + g] = x1; qr[10 + g] = x2;
;             }
	v_pk_mul_f32 v[34:35], v[26:27], v[30:31] op_sel:[0,1] op_sel_hi:[1,0]
	v_pk_mul_f32 v[26:27], v[26:27], v[30:31]
	v_sub_f32_e32 v28, v34, v35
	v_add_f32_e32 v26, v26, v27
	v_cvt_pk_bf16_f32 v27, v28, v193
	v_cvt_pk_bf16_f32 v26, v26, v193
	global_load_dwordx2 v[30:31], v[8:9], off offset:56
	v_and_b32_e32 v28, 0xffff0000, v33
	v_lshlrev_b32_e32 v35, 16, v0
	v_lshlrev_b32_e32 v34, 16, v4
	s_waitcnt vmcnt(0)
	v_pk_mul_f32 v[32:33], v[30:31], v[28:29] op_sel:[0,1] op_sel_hi:[1,0]
	v_pk_mul_f32 v[28:29], v[30:31], v[28:29]
	v_sub_f32_e32 v32, v32, v33
	v_add_f32_e32 v28, v28, v29
	v_cvt_pk_bf16_f32 v30, v32, v193
	v_cvt_pk_bf16_f32 v28, v28, v193
	global_load_dwordx2 v[32:33], v[8:9], off offset:128
	s_waitcnt vmcnt(0)
	v_pk_mul_f32 v[36:37], v[32:33], v[34:35] op_sel:[0,1] op_sel_hi:[1,0]
	v_pk_mul_f32 v[32:33], v[32:33], v[34:35]
	v_sub_f32_e32 v29, v36, v37
	v_add_f32_e32 v32, v32, v33
	v_cvt_pk_bf16_f32 v31, v29, v193
	v_cvt_pk_bf16_f32 v29, v32, v193
	global_load_dwordx2 v[32:33], v[8:9], off offset:136
	v_and_b32_e32 v35, 0xffff0000, v0
	v_and_b32_e32 v34, 0xffff0000, v4
	s_waitcnt vmcnt(0)
	v_pk_mul_f32 v[36:37], v[32:33], v[34:35] op_sel:[0,1] op_sel_hi:[1,0]
	v_pk_mul_f32 v[32:33], v[32:33], v[34:35]
	v_sub_f32_e32 v0, v36, v37
	v_add_f32_e32 v4, v32, v33
	v_cvt_pk_bf16_f32 v32, v0, v193
	v_cvt_pk_bf16_f32 v4, v4, v193
	global_load_dwordx2 v[34:35], v[8:9], off offset:144
	v_lshlrev_b32_e32 v37, 16, v1
	v_lshlrev_b32_e32 v36, 16, v5
	v_and_b32_e32 v1, 0xffff0000, v1
	s_waitcnt vmcnt(0)
	v_pk_mul_f32 v[38:39], v[34:35], v[36:37] op_sel:[0,1] op_sel_hi:[1,0]
	v_pk_mul_f32 v[34:35], v[34:35], v[36:37]
	v_sub_f32_e32 v0, v38, v39
	v_add_f32_e32 v33, v34, v35
	v_cvt_pk_bf16_f32 v34, v0, v193
	v_cvt_pk_bf16_f32 v33, v33, v193
	global_load_dwordx2 v[36:37], v[8:9], off offset:152
	v_and_b32_e32 v0, 0xffff0000, v5
	s_waitcnt vmcnt(0)
	v_pk_mul_f32 v[38:39], v[36:37], v[0:1] op_sel:[0,1] op_sel_hi:[1,0]
	v_pk_mul_f32 v[0:1], v[36:37], v[0:1]
	v_sub_f32_e32 v5, v38, v39
	v_add_f32_e32 v0, v0, v1
	v_cvt_pk_bf16_f32 v35, v5, v193
	v_cvt_pk_bf16_f32 v5, v0, v193
	global_load_dwordx2 v[0:1], v[8:9], off offset:160
	v_lshlrev_b32_e32 v37, 16, v2
	v_lshlrev_b32_e32 v36, 16, v6
	s_waitcnt vmcnt(0)
	v_pk_mul_f32 v[38:39], v[0:1], v[36:37] op_sel:[0,1] op_sel_hi:[1,0]
	v_pk_mul_f32 v[0:1], v[0:1], v[36:37]
	v_sub_f32_e32 v38, v38, v39
	v_add_f32_e32 v0, v0, v1
	v_cvt_pk_bf16_f32 v37, v38, v193
	v_cvt_pk_bf16_f32 v36, v0, v193
	global_load_dwordx2 v[0:1], v[8:9], off offset:168
	v_and_b32_e32 v39, 0xffff0000, v2
	v_and_b32_e32 v38, 0xffff0000, v6
	s_waitcnt vmcnt(0)
	v_pk_mul_f32 v[40:41], v[0:1], v[38:39] op_sel:[0,1] op_sel_hi:[1,0]
	v_pk_mul_f32 v[0:1], v[0:1], v[38:39]
	v_sub_f32_e32 v2, v40, v41
	v_add_f32_e32 v0, v0, v1
	v_cvt_pk_bf16_f32 v6, v2, v193
	v_cvt_pk_bf16_f32 v2, v0, v193
	global_load_dwordx2 v[0:1], v[8:9], off offset:176
	v_lshlrev_b32_e32 v39, 16, v3
	v_lshlrev_b32_e32 v38, 16, v7
	s_waitcnt vmcnt(0)
	v_pk_mul_f32 v[40:41], v[0:1], v[38:39] op_sel:[0,1] op_sel_hi:[1,0]
	v_pk_mul_f32 v[0:1], v[0:1], v[38:39]
	v_sub_f32_e32 v40, v40, v41
	v_add_f32_e32 v0, v0, v1
	v_cvt_pk_bf16_f32 v39, v40, v193
	v_cvt_pk_bf16_f32 v38, v0, v193
	global_load_dwordx2 v[0:1], v[8:9], off offset:184
	v_and_b32_e32 v9, 0xffff0000, v3
	v_and_b32_e32 v8, 0xffff0000, v7
	s_waitcnt vmcnt(0)
; #define VM_WAIT() asm volatile("s_waitcnt vmcnt(0)" ::: "memory")
;     ...
;         } else if constexpr (ATT_GLDS) {
;         unsigned gsv[2], gsk[2], gsk2 = 0u;
; #pragma unroll
;         for (int i = 0; i < 2; ++i) { const int a = (i * 512 + tid) * 16;
;             { const int sub = a >> 9, within = a & 511; const int kk = (sub >> 2) * 8 + (within >> 6); const int k = (kk & ~0xC) | ((kk & 4) << 1) | ((kk & 8) >> 1);
;               const int c = (sub & 3) * 32 + ((within & 63) >> 1); gsv[i] = (unsigned)(k * ldv + c) * 2u; }
;             if constexpr (MODE == MODE_DIFF) { if (i == 0) { const int row = a >> 7, ch = ((a >> 4) & 7) ^ ((row >> 1) & 7); gsk[0] = (unsigned)(row * ldk + ch * 8) * 2u; } gsk[1] = 0u; }
;             else { const int row = a >> 8, ch = ((a >> 4) & 15) ^ (row & 15); gsk[i] = (unsigned)(row * ldk + ch * 8) * 2u; } }
;         if constexpr (MODE == MODE_MLA) { const int a = tid * 16, row = a >> 7, ch = ((a >> 4) & 7) ^ ((row >> 1) & 7); gsk2 = (unsigned)(row * UW + ch * 8) * 2u; }
;         const unsigned ldsw = (unsigned)__builtin_amdgcn_readfirstlane(wid) * 1024u;
;     ...
;         GLDS(0, 0); VM_WAIT(); __syncthreads();
; #pragma unroll 1
;         for (int t = 0; t < NT; ++t) {
	v_pk_mul_f32 v[40:41], v[0:1], v[8:9] op_sel:[0,1] op_sel_hi:[1,0]
	v_pk_mul_f32 v[0:1], v[0:1], v[8:9]
	v_sub_f32_e32 v3, v40, v41
	v_add_f32_e32 v0, v0, v1
	v_bfe_i32 v9, v11, 4, 24
	v_cvt_pk_bf16_f32 v8, v3, v193
	v_cvt_pk_bf16_f32 v7, v0, v193
	v_bfe_u32 v0, v11, 2, 2
	v_lshrrev_b32_e32 v1, 1, v11
	v_lshlrev_b32_e32 v3, 1, v11
	v_lshrrev_b32_e32 v41, 1, v9
	v_and_or_b32 v0, v1, 8, v0
	v_and_b32_e32 v1, 0xc0, v3
	v_and_b32_e32 v40, 0xffff0, v9
	v_and_b32_e32 v41, 4, v41
	v_and_or_b32 v1, v13, 48, v1
	v_or3_b32 v40, v40, v41, v0
	v_lshl_or_b32 v192, v40, 12, v1
	v_xor_b32_e32 v40, v9, v11
	v_lshlrev_b32_e32 v9, 12, v9
	v_lshlrev_b32_e32 v40, 4, v40
	v_and_or_b32 v146, v40, s87, v9
	v_add_u32_e32 v9, 0x2000, v13
	v_ashrrev_i32_e32 v9, 8, v9
	v_lshrrev_b32_e32 v41, 1, v9
	v_and_b32_e32 v40, 0xffff0, v9
	v_and_b32_e32 v41, 4, v41
	v_or3_b32 v0, v40, v41, v0
	v_lshl_add_u64 v[40:41], s[0:1], 0, v[192:193]
	v_lshl_or_b32 v148, v0, 12, v1
	v_lshl_add_u64 v[40:41], v[40:41], 0, s[36:37]
	global_load_lds_dwordx4 v[40:41], off
	v_lshl_add_u64 v[40:41], s[0:1], 0, v[148:149]
	v_xor_b32_e32 v0, v9, v11
	v_lshl_add_u64 v[40:41], v[40:41], 0, s[36:37]
	s_add_i32 m0, s29, 0x2000
	v_lshlrev_b32_e32 v1, 12, v9
	v_lshlrev_b32_e32 v0, 4, v0
	global_load_lds_dwordx4 v[40:41], off
	s_mov_b32 m0, s2
	v_and_or_b32 v150, v0, s87, v1
	global_load_lds_dwordx4 v146, s[0:1]
	s_add_i32 m0, s29, 0xe000
	v_lshlrev_b32_e32 v0, 10, v11
	global_load_lds_dwordx4 v150, s[0:1]
	s_lshl_b64 s[0:1], s[4:5], 13
	v_and_b32_e32 v0, 0xffffe000, v0
	v_xor_b32_e32 v1, v13, v11
	s_add_u32 s0, s14, s0
	v_and_or_b32 v0, v1, s3, v0
	s_addc_u32 s1, s15, s1
	s_add_i32 m0, s29, 0x10000
	v_mov_b32_e32 v1, v193
	global_load_lds_dwordx4 v0, s[0:1]
	v_lshl_add_u64 v[152:153], s[14:15], 0, v[0:1]
	v_bitop3_b32 v0, v155, v11, 15 bitop3:0x78
	v_lshlrev_b32_e32 v9, 3, v11
	v_lshlrev_b32_e32 v158, 4, v0
	v_and_b32_e32 v0, 0xf0, v13
	v_bitop3_b32 v159, v144, v0, 32 bitop3:0x36
	v_bitop3_b32 v160, v144, v0, 64 bitop3:0x36
	v_bitop3_b32 v161, v144, v0, s60 bitop3:0x36
	v_bitop3_b32 v162, v144, v0, s59 bitop3:0x36
	v_bitop3_b32 v164, v144, v0, s61 bitop3:0x36
	v_bitop3_b32 v165, v144, v0, s58 bitop3:0x36
	v_bitop3_b32 v166, v144, v0, s62 bitop3:0x36
	v_and_b32_e32 v0, 0x70, v9
	v_bitop3_b32 v169, v144, v0, 32 bitop3:0x36
	v_bitop3_b32 v170, v144, v0, 64 bitop3:0x36
	v_bitop3_b32 v171, v144, v0, s60 bitop3:0x36
	v_and_b32_e32 v0, 0x118, v9
	s_mov_b32 s0, 0x5040100
	s_waitcnt vmcnt(0)
	v_perm_b32 v128, v17, v15, s0
	v_perm_b32 v136, v16, v14, s0
	v_and_or_b32 v0, v3, 32, v0
	v_mov_b32_e32 v14, v193
	v_mov_b32_e32 v15, v193
	v_bitop3_b32 v168, v144, v9, s3 bitop3:0x78
	v_cmp_gt_u32_e64 s[2:3], 32, v10
	v_perm_b32 v129, v21, v19, s0
	v_perm_b32 v130, v25, v23, s0
	v_perm_b32 v131, v30, v27, s0
	v_perm_b32 v132, v32, v31, s0
	v_perm_b32 v133, v35, v34, s0
	v_perm_b32 v134, v6, v37, s0
	v_perm_b32 v135, v8, v39, s0
	v_perm_b32 v137, v20, v18, s0
	v_perm_b32 v138, v24, v22, s0
	v_perm_b32 v139, v28, v26, s0
	v_perm_b32 v140, v4, v29, s0
	v_perm_b32 v141, v5, v33, s0
	v_perm_b32 v142, v2, v36, s0
	v_perm_b32 v143, v7, v38, s0
	v_add3_u32 v172, v12, 0, v0
	v_mov_b32_e32 v0, v193
	v_mov_b32_e32 v2, v193
	v_mov_b32_e32 v3, v193
	v_mov_b32_e32 v4, v193
	v_mov_b32_e32 v5, v193
	v_mov_b32_e32 v6, v193
	v_mov_b32_e32 v7, v193
	v_mov_b32_e32 v8, v193
	v_mov_b32_e32 v9, v193
	v_mov_b32_e32 v10, v193
	v_mov_b32_e32 v11, v193
	v_mov_b32_e32 v12, v193
	v_mov_b32_e32 v13, v193
	v_mov_b64_e32 v[30:31], v[14:15]
	v_mov_b64_e32 v[46:47], v[14:15]
	v_mov_b64_e32 v[62:63], v[14:15]
	s_or_b32 s16, s4, 64
	v_mov_b64_e32 v[28:29], v[12:13]
	v_mov_b64_e32 v[26:27], v[10:11]
	v_mov_b64_e32 v[24:25], v[8:9]
	v_mov_b64_e32 v[22:23], v[6:7]
	v_mov_b64_e32 v[20:21], v[4:5]
	v_mov_b64_e32 v[18:19], v[2:3]
	v_mov_b64_e32 v[16:17], v[0:1]
	v_mov_b64_e32 v[44:45], v[12:13]
	v_mov_b64_e32 v[42:43], v[10:11]
	v_mov_b64_e32 v[40:41], v[8:9]
	v_mov_b64_e32 v[38:39], v[6:7]
	v_mov_b64_e32 v[36:37], v[4:5]
	v_mov_b64_e32 v[34:35], v[2:3]
	v_mov_b64_e32 v[32:33], v[0:1]
	v_mov_b64_e32 v[60:61], v[12:13]
	v_mov_b64_e32 v[58:59], v[10:11]
	v_mov_b64_e32 v[56:57], v[8:9]
	v_mov_b64_e32 v[54:55], v[6:7]
	v_mov_b64_e32 v[52:53], v[4:5]
	v_mov_b64_e32 v[50:51], v[2:3]
	v_mov_b64_e32 v[48:49], v[0:1]
	s_waitcnt vmcnt(0) lgkmcnt(0)
	s_barrier
	s_mov_b32 s30, 0
	s_branch .LBB0_787

; #define VM_WAIT() asm volatile("s_waitcnt vmcnt(0)" ::: "memory")
;     ...
;             VM_WAIT();
;             __syncthreads();
.Lilc_n_m:
	s_cmp_eq_u32 s42, 0
	s_cbranch_scc1 .Lilc_np_m
	s_cmp_eq_u32 s53, 0
	s_cbranch_scc1 .Lilc_p_m
	s_cmp_eq_u32 s50, 0
	s_cbranch_scc1 .Lilc_np_m
	s_cmp_lt_u32 s28, 62
	s_cbranch_scc1 .Lpfx_5
	s_waitcnt vmcnt(0)
	s_branch .Lilc_p_m

; #define SBAR() __builtin_amdgcn_sched_barrier(0)
; template <int MODE>
; __device__ __forceinline__ void partialSM(f32x16& p0, f32x16& p1, float& m_reg, float& mn, float& alpha) {
;     ...
;     const float mnC = -mn * C;
; #pragma unroll
;     for (int r = 0; r < 16; ++r) p0[r] = fmaf(p0[r], C, mnC);
; #pragma unroll
;     for (int r = 0; r < 16; ++r) p1[r] = fmaf(p1[r], C, mnC);
; #pragma unroll
;     for (int r = 0; r < 16; ++r) p0[r] = __builtin_amdgcn_exp2f(p0[r]);
; }
; __device__ __forceinline__ void finishSM(f32x16& p0, f32x16& p1, float alpha, float& l_reg, bf16x8& pa0, bf16x8& pa1, bf16x8& pa2, bf16x8& pa3) {
; #pragma unroll
;     for (int r = 0; r < 16; ++r) p1[r] = __builtin_amdgcn_exp2f(p1[r]);
;     float ps = 0;
; #pragma unroll
;     for (int r = 0; r < 16; ++r) ps += p0[r];
; #pragma unroll
;     for (int r = 0; r < 16; ++r) ps += p1[r];
;     { auto rr = __builtin_amdgcn_permlane32_swap(__float_as_uint(ps), __float_as_uint(ps), false, false);
;       ps = __uint_as_float(rr[0]) + __uint_as_float(rr[1]); }
;     l_reg = l_reg * alpha + ps;
;     ...
;     PK4(p0, 0, pa0); PK4(p0, 8, pa1); PK4(p1, 0, pa2); PK4(p1, 8, pa3);
;     ...
; }
; template <int D0> __device__ __forceinline__ void pv_one(f32x16& od, int vb, bf16x8 pa0, bf16x8 pa1, bf16x8 pa2, bf16x8 pa3) {
;     const s16x4 l0 = tr_read<v_rd_off(D0, 0, 0)>(vb), h0 = tr_read<v_rd_off(D0, 0, 1)>(vb), l1 = tr_read<v_rd_off(D0, 1, 0)>(vb), h1 = tr_read<v_rd_off(D0, 1, 1)>(vb);
;     const s16x4 l2 = tr_read<v_rd_off(D0, 2, 0)>(vb), h2 = tr_read<v_rd_off(D0, 2, 1)>(vb), l3 = tr_read<v_rd_off(D0, 3, 0)>(vb), h3 = tr_read<v_rd_off(D0, 3, 1)>(vb);
;     asm volatile("s_waitcnt lgkmcnt(0)" ::: "memory"); SBAR();
;     ...
;     od = __builtin_amdgcn_mfma_f32_32x32x16_bf16(pa0, PK(l0, h0), od, 0, 0, 0);
;     od = __builtin_amdgcn_mfma_f32_32x32x16_bf16(pa1, PK(l1, h1), od, 0, 0, 0);
;     od = __builtin_amdgcn_mfma_f32_32x32x16_bf16(pa2, PK(l2, h2), od, 0, 0, 0);
;     od = __builtin_amdgcn_mfma_f32_32x32x16_bf16(pa3, PK(l3, h3), od, 0, 0, 0);
;     ...
; }
; __device__ __forceinline__ void pv_d0(f32x16* o, int vb, bf16x8 pa0, bf16x8 pa1, bf16x8 pa2, bf16x8 pa3) {
;     pv_one<0>(o[0], vb, pa0, pa1, pa2, pa3); pv_one<1>(o[1], vb, pa0, pa1, pa2, pa3); pv_one<2>(o[2], vb, pa0, pa1, pa2, pa3); pv_one<3>(o[3], vb, pa0, pa1, pa2, pa3);
; }
.LBB0_792:
	v_cndmask_b32_e64 v173, v176, v173, s[4:5]
	v_mul_f32_e32 v176, 0xbdd53b94, v173
	v_fmamk_f32 v80, v80, 0x3dd53b94, v176
	v_fmamk_f32 v81, v81, 0x3dd53b94, v176
	v_fmamk_f32 v82, v82, 0x3dd53b94, v176
	v_fmamk_f32 v83, v83, 0x3dd53b94, v176
	v_fmamk_f32 v84, v84, 0x3dd53b94, v176
	v_fmamk_f32 v85, v85, 0x3dd53b94, v176
	v_fmamk_f32 v86, v86, 0x3dd53b94, v176
	v_fmamk_f32 v87, v87, 0x3dd53b94, v176
	v_fmamk_f32 v88, v88, 0x3dd53b94, v176
	v_fmamk_f32 v89, v89, 0x3dd53b94, v176
	v_fmamk_f32 v90, v90, 0x3dd53b94, v176
	v_fmamk_f32 v91, v91, 0x3dd53b94, v176
	v_fmamk_f32 v92, v92, 0x3dd53b94, v176
	v_fmamk_f32 v93, v93, 0x3dd53b94, v176
	v_fmamk_f32 v94, v94, 0x3dd53b94, v176
	v_fmamk_f32 v95, v95, 0x3dd53b94, v176
	v_fmamk_f32 v64, v64, 0x3dd53b94, v176
	v_fmamk_f32 v65, v65, 0x3dd53b94, v176
	v_fmamk_f32 v66, v66, 0x3dd53b94, v176
	v_fmamk_f32 v67, v67, 0x3dd53b94, v176
	v_fmamk_f32 v68, v68, 0x3dd53b94, v176
	v_fmamk_f32 v69, v69, 0x3dd53b94, v176
	v_fmamk_f32 v70, v70, 0x3dd53b94, v176
	v_fmamk_f32 v71, v71, 0x3dd53b94, v176
	v_fmamk_f32 v72, v72, 0x3dd53b94, v176
	v_fmamk_f32 v73, v73, 0x3dd53b94, v176
	v_fmamk_f32 v74, v74, 0x3dd53b94, v176
	v_fmamk_f32 v75, v75, 0x3dd53b94, v176
	v_fmamk_f32 v76, v76, 0x3dd53b94, v176
	v_fmamk_f32 v77, v77, 0x3dd53b94, v176
	v_fmamk_f32 v78, v78, 0x3dd53b94, v176
	v_fmac_f32_e32 v176, 0x3dd53b94, v79
	v_exp_f32_e32 v79, v80
	v_exp_f32_e32 v80, v81
	v_exp_f32_e32 v81, v82
	v_exp_f32_e32 v82, v83
	v_exp_f32_e32 v83, v84
	v_exp_f32_e32 v84, v85
	v_exp_f32_e32 v85, v86
	v_exp_f32_e32 v86, v87
	v_exp_f32_e32 v87, v88
	v_exp_f32_e32 v88, v89
	v_exp_f32_e32 v89, v90
	v_exp_f32_e32 v90, v91
	v_exp_f32_e32 v91, v92
	v_exp_f32_e32 v92, v93
	v_exp_f32_e32 v93, v94
	v_exp_f32_e32 v94, v95
	v_exp_f32_e32 v95, v64
	v_add_f32_e32 v64, 0, v79
	v_add_f32_e32 v64, v80, v64
	v_add_f32_e32 v64, v81, v64
	v_add_f32_e32 v64, v82, v64
	v_add_f32_e32 v64, v83, v64
	v_add_f32_e32 v64, v84, v64
	v_add_f32_e32 v64, v85, v64
	v_add_f32_e32 v64, v86, v64
	v_add_f32_e32 v64, v87, v64
	v_add_f32_e32 v64, v88, v64
	v_add_f32_e32 v64, v89, v64
	v_add_f32_e32 v64, v90, v64
	v_add_f32_e32 v64, v91, v64
	v_exp_f32_e32 v65, v65
	v_add_f32_e32 v64, v92, v64
	v_exp_f32_e32 v177, v66
	v_add_f32_e32 v64, v93, v64
	v_exp_f32_e32 v178, v67
	v_add_f32_e32 v64, v94, v64
	v_exp_f32_e32 v179, v68
	v_add_f32_e32 v64, v95, v64
	v_exp_f32_e32 v180, v69
	v_add_f32_e32 v64, v65, v64
	v_exp_f32_e32 v181, v70
	v_add_f32_e32 v64, v177, v64
	v_exp_f32_e32 v182, v71
	v_add_f32_e32 v64, v178, v64
	v_exp_f32_e32 v183, v72
	v_add_f32_e32 v64, v179, v64
	v_exp_f32_e32 v184, v73
	v_add_f32_e32 v64, v180, v64
	v_exp_f32_e32 v185, v74
	v_add_f32_e32 v64, v181, v64
	v_exp_f32_e32 v186, v75
	v_add_f32_e32 v64, v182, v64
	v_exp_f32_e32 v187, v76
	v_add_f32_e32 v64, v183, v64
	v_exp_f32_e32 v188, v77
	v_add_f32_e32 v64, v184, v64
	v_exp_f32_e32 v189, v78
	v_add_f32_e32 v64, v185, v64
	v_exp_f32_e32 v176, v176
	v_add_f32_e32 v64, v186, v64
	v_add_f32_e32 v64, v187, v64
	v_add_f32_e32 v64, v188, v64
	v_add_f32_e32 v64, v189, v64
	v_add_f32_e32 v64, v176, v64
	v_mov_b32_e32 v66, v64
	s_nop 1
	v_permlane32_swap_b32_e32 v64, v66
	v_add_f32_e32 v64, v64, v66
	s_add_i32 s28, s28, 1
	v_fmac_f32_e32 v64, v174, v175
	v_cvt_pk_bf16_f32 v66, v79, v80
	v_cvt_pk_bf16_f32 v67, v81, v82
	v_cvt_pk_bf16_f32 v68, v83, v84
	v_cvt_pk_bf16_f32 v69, v85, v86
	v_cvt_pk_bf16_f32 v70, v87, v88
	v_cvt_pk_bf16_f32 v71, v89, v90
	v_cvt_pk_bf16_f32 v72, v91, v92
	v_cvt_pk_bf16_f32 v73, v93, v94
	v_cvt_pk_bf16_f32 v74, v95, v65
	v_cvt_pk_bf16_f32 v75, v177, v178
	v_cvt_pk_bf16_f32 v76, v179, v180
	v_cvt_pk_bf16_f32 v77, v181, v182
	v_cvt_pk_bf16_f32 v78, v183, v184
	v_cvt_pk_bf16_f32 v79, v185, v186
	v_cvt_pk_bf16_f32 v80, v187, v188
	v_cvt_pk_bf16_f32 v81, v189, v176
	s_nop 0
	v_permlane32_swap_b32_e32 v66, v68
	v_permlane32_swap_b32_e32 v67, v69
	v_permlane32_swap_b32_e32 v70, v72
	v_permlane32_swap_b32_e32 v71, v73
	v_permlane32_swap_b32_e32 v74, v76
	v_permlane32_swap_b32_e32 v75, v77
	v_permlane32_swap_b32_e32 v78, v80
	v_permlane32_swap_b32_e32 v79, v81
	v_lshl_add_u32 v65, s30, 14, v172
	ds_read_b64_tr_b16 v[82:83], v65 offset:0
	ds_read_b64_tr_b16 v[84:85], v65 offset:0x800
	ds_read_b64_tr_b16 v[86:87], v65 offset:0x1000
	ds_read_b64_tr_b16 v[88:89], v65 offset:0x1800
	ds_read_b64_tr_b16 v[90:91], v65 offset:0x2000
	ds_read_b64_tr_b16 v[92:93], v65 offset:0x2800
	ds_read_b64_tr_b16 v[174:175], v65 offset:0x3000
	ds_read_b64_tr_b16 v[176:177], v65 offset:0x3800
	s_waitcnt lgkmcnt(0)
	s_nop 0
	v_mfma_f32_32x32x16_bf16 v[0:15], v[66:69], v[82:85], v[0:15]
	ds_read_b64_tr_b16 v[82:83], v65 offset:0x200
	ds_read_b64_tr_b16 v[84:85], v65 offset:0xa00
	v_mfma_f32_32x32x16_bf16 v[0:15], v[70:73], v[86:89], v[0:15]
	ds_read_b64_tr_b16 v[86:87], v65 offset:0x1200
	ds_read_b64_tr_b16 v[88:89], v65 offset:0x1a00
	v_mfma_f32_32x32x16_bf16 v[0:15], v[74:77], v[90:93], v[0:15]
	ds_read_b64_tr_b16 v[90:91], v65 offset:0x2200
	ds_read_b64_tr_b16 v[92:93], v65 offset:0x2a00
	v_mfma_f32_32x32x16_bf16 v[0:15], v[78:81], v[174:177], v[0:15]
	ds_read_b64_tr_b16 v[174:175], v65 offset:0x3200
	ds_read_b64_tr_b16 v[176:177], v65 offset:0x3a00
	s_waitcnt lgkmcnt(0)
	v_mfma_f32_32x32x16_bf16 v[16:31], v[66:69], v[82:85], v[16:31]
	ds_read_b64_tr_b16 v[82:83], v65 offset:0x400
	ds_read_b64_tr_b16 v[84:85], v65 offset:0xc00
	v_mfma_f32_32x32x16_bf16 v[16:31], v[70:73], v[86:89], v[16:31]
	ds_read_b64_tr_b16 v[86:87], v65 offset:0x1400
	ds_read_b64_tr_b16 v[88:89], v65 offset:0x1c00
	v_mfma_f32_32x32x16_bf16 v[16:31], v[74:77], v[90:93], v[16:31]
	ds_read_b64_tr_b16 v[90:91], v65 offset:0x2400
	ds_read_b64_tr_b16 v[92:93], v65 offset:0x2c00
	v_mfma_f32_32x32x16_bf16 v[16:31], v[78:81], v[174:177], v[16:31]
	ds_read_b64_tr_b16 v[174:175], v65 offset:0x3400
	ds_read_b64_tr_b16 v[176:177], v65 offset:0x3c00
	s_waitcnt lgkmcnt(0)
	v_mfma_f32_32x32x16_bf16 v[32:47], v[66:69], v[82:85], v[32:47]
	ds_read_b64_tr_b16 v[82:83], v65 offset:0x600
	ds_read_b64_tr_b16 v[84:85], v65 offset:0xe00
	v_mfma_f32_32x32x16_bf16 v[32:47], v[70:73], v[86:89], v[32:47]
	ds_read_b64_tr_b16 v[86:87], v65 offset:0x1600
	ds_read_b64_tr_b16 v[88:89], v65 offset:0x1e00
	v_mfma_f32_32x32x16_bf16 v[32:47], v[74:77], v[90:93], v[32:47]
	ds_read_b64_tr_b16 v[90:91], v65 offset:0x2600
	ds_read_b64_tr_b16 v[92:93], v65 offset:0x2e00
	v_mfma_f32_32x32x16_bf16 v[32:47], v[78:81], v[174:177], v[32:47]
	ds_read_b64_tr_b16 v[174:175], v65 offset:0x3600
	ds_read_b64_tr_b16 v[176:177], v65 offset:0x3e00
	s_waitcnt lgkmcnt(0)
	v_mfma_f32_32x32x16_bf16 v[48:63], v[66:69], v[82:85], v[48:63]
	s_cmp_lt_u32 s28, 63
	s_cbranch_scc0 .Lpfw_nd
	s_cmp_eq_u32 s53, 12
	s_cbranch_scc1 .Lpfw_17
	s_cmp_eq_u32 s53, 8
	s_cbranch_scc1 .Lpfw_13
	s_waitcnt vmcnt(5)
	s_branch .Lpfw_d
.Lpfw_17:
	s_waitcnt vmcnt(17)
	s_branch .Lpfw_d
.Lpfw_13:
	s_waitcnt vmcnt(13)
	s_branch .Lpfw_d
.Lpfw_nd:
	s_cmp_eq_u32 s53, 12
	s_cbranch_scc1 .Lpfw_12
	s_cmp_eq_u32 s53, 8
	s_cbranch_scc1 .Lpfw_8
	s_waitcnt vmcnt(0)
	s_branch .Lpfw_d
